# v33 + write-through (sc1) output stores in the residual GEMM epilogues of P1, P4, P9 (2 units per CU each)
# speedup vs baseline: 1.0006x; 1.0006x over previous
.LBB0_352:
	s_mov_b64 s[98:99], 0x20000
	s_lshl_b32 s2, s36, 8
	s_add_i32 s2, s2, s49
	v_and_or_b32 v164, v164, 15, s2
	v_ashrrev_i32_e32 v165, 31, v164
	v_lshlrev_b64 v[160:161], 11, v[164:165]
	v_lshl_add_u64 v[160:161], v[160:161], 0, v[162:163]
	v_lshl_add_u64 v[178:179], v[160:161], 2, s[6:7]
	global_load_dwordx4 v[170:173], v[178:179], off
	global_load_dwordx4 v[174:177], v[178:179], off offset:16
	global_load_dwordx4 v[182:185], v[178:179], off offset:512
	global_load_dwordx4 v[186:189], v[178:179], off offset:528
	v_lshl_add_u64 v[246:247], v[178:179], 0, s[98:99]
	global_load_dwordx4 v[190:193], v[246:247], off
	global_load_dwordx4 v[194:197], v[246:247], off offset:16
	v_lshl_add_u64 v[246:247], v[178:179], 0, s[98:99]
	global_load_dwordx4 v[198:201], v[246:247], off offset:512
	global_load_dwordx4 v[202:205], v[246:247], off offset:528
	v_lshl_add_u64 v[246:247], v[178:179], 0, s[98:99]
	v_lshl_add_u64 v[246:247], v[246:247], 0, s[98:99]
	global_load_dwordx4 v[206:209], v[246:247], off
	global_load_dwordx4 v[210:213], v[246:247], off offset:16
	v_lshl_add_u64 v[246:247], v[178:179], 0, s[98:99]
	v_lshl_add_u64 v[246:247], v[246:247], 0, s[98:99]
	global_load_dwordx4 v[214:217], v[246:247], off offset:512
	global_load_dwordx4 v[218:221], v[246:247], off offset:528
	v_lshl_add_u64 v[246:247], v[178:179], 0, s[98:99]
	v_lshl_add_u64 v[246:247], v[246:247], 0, s[98:99]
	v_lshl_add_u64 v[246:247], v[246:247], 0, s[98:99]
	global_load_dwordx4 v[222:225], v[246:247], off
	global_load_dwordx4 v[226:229], v[246:247], off offset:16
	v_lshl_add_u64 v[246:247], v[178:179], 0, s[98:99]
	v_lshl_add_u64 v[246:247], v[246:247], 0, s[98:99]
	v_lshl_add_u64 v[246:247], v[246:247], 0, s[98:99]
	global_load_dwordx4 v[230:233], v[246:247], off offset:512
	global_load_dwordx4 v[234:237], v[246:247], off offset:528
	v_lshl_add_u64 v[246:247], v[160:161], 0, s[20:21]
	v_lshl_add_u64 v[246:247], v[246:247], 2, s[6:7]
	global_load_dwordx4 v[238:241], v[246:247], off
	global_load_dwordx4 v[242:245], v[246:247], off offset:16
	v_lshl_add_u64 v[180:181], v[160:161], 1, s[64:65]
	s_andn2_b64 vcc, exec, s[0:1]
	s_mov_b64 s[0:1], -1
	s_waitcnt vmcnt(16)
	v_pk_mul_f32 v[170:171], v[170:171], s[18:19] op_sel_hi:[1,0]
	v_pk_mul_f32 v[176:177], v[176:177], s[18:19] op_sel_hi:[1,0]
	v_pk_mul_f32 v[174:175], v[174:175], s[18:19] op_sel_hi:[1,0]
	v_pk_mul_f32 v[172:173], v[172:173], s[18:19] op_sel_hi:[1,0]
	v_pk_fma_f32 v[140:141], v[140:141], v[132:133], v[170:171]
	v_pk_fma_f32 v[170:171], v[138:139], v[130:131], v[176:177]
	v_pk_fma_f32 v[138:139], v[136:137], v[128:129], v[174:175]
	v_pk_fma_f32 v[142:143], v[142:143], v[134:135], v[172:173]
	v_cvt_pk_bf16_f32 v136, v140, v141
	s_nop 0
	v_cvt_pk_bf16_f32 v137, v142, v143
	v_cvt_pk_bf16_f32 v138, v138, v139
	v_cvt_pk_bf16_f32 v139, v170, v171
	global_store_dwordx4 v[180:181], v[136:139], off sc1
	s_nop 1
	v_or_b32_e32 v170, 16, v164
	v_ashrrev_i32_e32 v171, 31, v170
	v_lshlrev_b64 v[170:171], 11, v[170:171]
	v_lshl_add_u64 v[170:171], v[170:171], 0, v[162:163]
	s_waitcnt vmcnt(16)
	v_pk_mul_f32 v[136:137], v[182:183], s[18:19] op_sel_hi:[1,0]
	s_waitcnt vmcnt(15)
	v_pk_mul_f32 v[142:143], v[188:189], s[18:19] op_sel_hi:[1,0]
	v_pk_mul_f32 v[140:141], v[186:187], s[18:19] op_sel_hi:[1,0]
	v_pk_mul_f32 v[138:139], v[184:185], s[18:19] op_sel_hi:[1,0]
	v_lshl_add_u64 v[246:247], v[160:161], 0, s[20:21]
	v_lshl_add_u64 v[246:247], v[246:247], 2, s[6:7]
	global_load_dwordx4 v[182:185], v[246:247], off offset:512
	global_load_dwordx4 v[186:189], v[246:247], off offset:528
	v_pk_fma_f32 v[116:117], v[116:117], v[124:125], v[136:137]
	v_pk_fma_f32 v[136:137], v[114:115], v[122:123], v[142:143]
	v_pk_fma_f32 v[114:115], v[112:113], v[120:121], v[140:141]
	v_pk_fma_f32 v[118:119], v[118:119], v[126:127], v[138:139]
	v_cvt_pk_bf16_f32 v112, v116, v117
	s_nop 0
	v_cvt_pk_bf16_f32 v113, v118, v119
	v_cvt_pk_bf16_f32 v114, v114, v115
	v_cvt_pk_bf16_f32 v115, v136, v137
	global_store_dwordx4 v[180:181], v[112:115], off offset:256 sc1
	s_nop 1
	v_lshl_add_u64 v[136:137], v[170:171], 1, s[64:65]
	s_waitcnt vmcnt(17)
	v_pk_mul_f32 v[112:113], v[190:191], s[18:19] op_sel_hi:[1,0]
	s_waitcnt vmcnt(16)
	v_pk_mul_f32 v[118:119], v[196:197], s[18:19] op_sel_hi:[1,0]
	v_pk_mul_f32 v[116:117], v[194:195], s[18:19] op_sel_hi:[1,0]
	v_pk_mul_f32 v[114:115], v[192:193], s[18:19] op_sel_hi:[1,0]
	v_lshl_add_u64 v[246:247], v[160:161], 0, s[22:23]
	v_lshl_add_u64 v[246:247], v[246:247], 2, s[6:7]
	global_load_dwordx4 v[190:193], v[246:247], off
	global_load_dwordx4 v[194:197], v[246:247], off offset:16
	v_pk_fma_f32 v[108:109], v[108:109], v[132:133], v[112:113]
	v_pk_fma_f32 v[112:113], v[106:107], v[130:131], v[118:119]
	v_pk_fma_f32 v[106:107], v[104:105], v[128:129], v[116:117]
	v_pk_fma_f32 v[110:111], v[110:111], v[134:135], v[114:115]
	v_cvt_pk_bf16_f32 v104, v108, v109
	s_nop 0
	v_cvt_pk_bf16_f32 v105, v110, v111
	v_cvt_pk_bf16_f32 v106, v106, v107
	v_cvt_pk_bf16_f32 v107, v112, v113
	global_store_dwordx4 v[136:137], v[104:107], off sc1
	s_nop 1
	v_or_b32_e32 v112, 32, v164
	v_ashrrev_i32_e32 v113, 31, v112
	v_lshlrev_b64 v[112:113], 11, v[112:113]
	v_lshl_add_u64 v[112:113], v[112:113], 0, v[162:163]
	s_waitcnt vmcnt(18)
	v_pk_mul_f32 v[104:105], v[198:199], s[18:19] op_sel_hi:[1,0]
	s_waitcnt vmcnt(17)
	v_pk_mul_f32 v[110:111], v[204:205], s[18:19] op_sel_hi:[1,0]
	v_pk_mul_f32 v[108:109], v[202:203], s[18:19] op_sel_hi:[1,0]
	v_pk_mul_f32 v[106:107], v[200:201], s[18:19] op_sel_hi:[1,0]
	v_lshl_add_u64 v[246:247], v[160:161], 0, s[22:23]
	v_lshl_add_u64 v[246:247], v[246:247], 2, s[6:7]
	global_load_dwordx4 v[198:201], v[246:247], off offset:512
	global_load_dwordx4 v[202:205], v[246:247], off offset:528
	v_pk_fma_f32 v[100:101], v[100:101], v[124:125], v[104:105]
	v_pk_fma_f32 v[104:105], v[98:99], v[122:123], v[110:111]
	v_pk_fma_f32 v[98:99], v[96:97], v[120:121], v[108:109]
	v_pk_fma_f32 v[102:103], v[102:103], v[126:127], v[106:107]
	v_cvt_pk_bf16_f32 v96, v100, v101
	s_nop 0
	v_cvt_pk_bf16_f32 v97, v102, v103
	v_cvt_pk_bf16_f32 v98, v98, v99
	v_cvt_pk_bf16_f32 v99, v104, v105
	global_store_dwordx4 v[136:137], v[96:99], off offset:256 sc1
	s_nop 1
	v_lshl_add_u64 v[104:105], v[112:113], 1, s[64:65]
	s_waitcnt vmcnt(19)
	v_pk_mul_f32 v[96:97], v[206:207], s[18:19] op_sel_hi:[1,0]
	s_waitcnt vmcnt(18)
	v_pk_mul_f32 v[102:103], v[212:213], s[18:19] op_sel_hi:[1,0]
	v_pk_mul_f32 v[100:101], v[210:211], s[18:19] op_sel_hi:[1,0]
	v_pk_mul_f32 v[98:99], v[208:209], s[18:19] op_sel_hi:[1,0]
	v_lshl_add_u64 v[246:247], v[160:161], 0, s[24:25]
	v_lshl_add_u64 v[246:247], v[246:247], 2, s[6:7]
	global_load_dwordx4 v[206:209], v[246:247], off
	global_load_dwordx4 v[210:213], v[246:247], off offset:16
	v_pk_fma_f32 v[92:93], v[92:93], v[132:133], v[96:97]
	v_pk_fma_f32 v[96:97], v[90:91], v[130:131], v[102:103]
	v_pk_fma_f32 v[90:91], v[88:89], v[128:129], v[100:101]
	v_pk_fma_f32 v[94:95], v[94:95], v[134:135], v[98:99]
	v_cvt_pk_bf16_f32 v88, v92, v93
	s_nop 0
	v_cvt_pk_bf16_f32 v89, v94, v95
	v_cvt_pk_bf16_f32 v90, v90, v91
	v_cvt_pk_bf16_f32 v91, v96, v97
	global_store_dwordx4 v[104:105], v[88:91], off sc1
	s_nop 1
	v_or_b32_e32 v96, 48, v164
	v_ashrrev_i32_e32 v97, 31, v96
	v_lshlrev_b64 v[96:97], 11, v[96:97]
	v_lshl_add_u64 v[96:97], v[96:97], 0, v[162:163]
	s_waitcnt vmcnt(20)
	v_pk_mul_f32 v[88:89], v[214:215], s[18:19] op_sel_hi:[1,0]
	s_waitcnt vmcnt(19)
	v_pk_mul_f32 v[94:95], v[220:221], s[18:19] op_sel_hi:[1,0]
	v_pk_mul_f32 v[92:93], v[218:219], s[18:19] op_sel_hi:[1,0]
	v_pk_mul_f32 v[90:91], v[216:217], s[18:19] op_sel_hi:[1,0]
	v_lshl_add_u64 v[246:247], v[160:161], 0, s[24:25]
	v_lshl_add_u64 v[246:247], v[246:247], 2, s[6:7]
	global_load_dwordx4 v[214:217], v[246:247], off offset:512
	global_load_dwordx4 v[218:221], v[246:247], off offset:528
	v_pk_fma_f32 v[84:85], v[84:85], v[124:125], v[88:89]
	v_pk_fma_f32 v[88:89], v[82:83], v[122:123], v[94:95]
	v_pk_fma_f32 v[82:83], v[80:81], v[120:121], v[92:93]
	v_pk_fma_f32 v[86:87], v[86:87], v[126:127], v[90:91]
	v_cvt_pk_bf16_f32 v80, v84, v85
	s_nop 0
	v_cvt_pk_bf16_f32 v81, v86, v87
	v_cvt_pk_bf16_f32 v82, v82, v83
	v_cvt_pk_bf16_f32 v83, v88, v89
	global_store_dwordx4 v[104:105], v[80:83], off offset:256 sc1
	s_nop 1
	v_lshl_add_u64 v[88:89], v[96:97], 1, s[64:65]
	s_waitcnt vmcnt(21)
	v_pk_mul_f32 v[80:81], v[222:223], s[18:19] op_sel_hi:[1,0]
	s_waitcnt vmcnt(20)
	v_pk_mul_f32 v[86:87], v[228:229], s[18:19] op_sel_hi:[1,0]
	v_pk_mul_f32 v[84:85], v[226:227], s[18:19] op_sel_hi:[1,0]
	v_pk_mul_f32 v[82:83], v[224:225], s[18:19] op_sel_hi:[1,0]
	v_lshl_add_u64 v[246:247], v[160:161], 0, s[26:27]
	v_lshl_add_u64 v[246:247], v[246:247], 2, s[6:7]
	global_load_dwordx4 v[222:225], v[246:247], off
	global_load_dwordx4 v[226:229], v[246:247], off offset:16
	v_pk_fma_f32 v[76:77], v[76:77], v[132:133], v[80:81]
	v_pk_fma_f32 v[80:81], v[74:75], v[130:131], v[86:87]
	v_pk_fma_f32 v[74:75], v[72:73], v[128:129], v[84:85]
	v_pk_fma_f32 v[78:79], v[78:79], v[134:135], v[82:83]
	v_cvt_pk_bf16_f32 v72, v76, v77
	s_nop 0
	v_cvt_pk_bf16_f32 v73, v78, v79
	v_cvt_pk_bf16_f32 v74, v74, v75
	v_cvt_pk_bf16_f32 v75, v80, v81
	global_store_dwordx4 v[88:89], v[72:75], off sc1
	s_nop 1
	v_lshl_add_u64 v[80:81], v[160:161], 0, s[20:21]
	s_waitcnt vmcnt(22)
	v_pk_mul_f32 v[72:73], v[230:231], s[18:19] op_sel_hi:[1,0]
	s_waitcnt vmcnt(21)
	v_pk_mul_f32 v[78:79], v[236:237], s[18:19] op_sel_hi:[1,0]
	v_pk_mul_f32 v[76:77], v[234:235], s[18:19] op_sel_hi:[1,0]
	v_pk_mul_f32 v[74:75], v[232:233], s[18:19] op_sel_hi:[1,0]
	v_lshl_add_u64 v[246:247], v[160:161], 0, s[26:27]
	v_lshl_add_u64 v[246:247], v[246:247], 2, s[6:7]
	global_load_dwordx4 v[230:233], v[246:247], off offset:512
	global_load_dwordx4 v[234:237], v[246:247], off offset:528
	v_pk_fma_f32 v[68:69], v[68:69], v[124:125], v[72:73]
	v_pk_fma_f32 v[72:73], v[66:67], v[122:123], v[78:79]
	v_pk_fma_f32 v[66:67], v[64:65], v[120:121], v[76:77]
	v_pk_fma_f32 v[70:71], v[70:71], v[126:127], v[74:75]
	v_cvt_pk_bf16_f32 v64, v68, v69
	s_nop 0
	v_cvt_pk_bf16_f32 v65, v70, v71
	v_cvt_pk_bf16_f32 v66, v66, v67
	v_cvt_pk_bf16_f32 v67, v72, v73
	global_store_dwordx4 v[88:89], v[64:67], off offset:256 sc1
	s_nop 1
	v_lshl_add_u64 v[72:73], v[80:81], 1, s[64:65]
	s_waitcnt vmcnt(23)
	v_pk_mul_f32 v[64:65], v[238:239], s[18:19] op_sel_hi:[1,0]
	s_waitcnt vmcnt(22)
	v_pk_mul_f32 v[70:71], v[244:245], s[18:19] op_sel_hi:[1,0]
	v_pk_mul_f32 v[68:69], v[242:243], s[18:19] op_sel_hi:[1,0]
	v_pk_mul_f32 v[66:67], v[240:241], s[18:19] op_sel_hi:[1,0]
	v_pk_fma_f32 v[60:61], v[60:61], v[132:133], v[64:65]
	v_pk_fma_f32 v[64:65], v[58:59], v[130:131], v[70:71]
	v_pk_fma_f32 v[58:59], v[56:57], v[128:129], v[68:69]
	v_pk_fma_f32 v[62:63], v[62:63], v[134:135], v[66:67]
	v_cvt_pk_bf16_f32 v56, v60, v61
	s_nop 0
	v_cvt_pk_bf16_f32 v57, v62, v63
	v_cvt_pk_bf16_f32 v58, v58, v59
	v_cvt_pk_bf16_f32 v59, v64, v65
	global_store_dwordx4 v[72:73], v[56:59], off sc1
	s_nop 1
	v_lshl_add_u64 v[64:65], v[160:161], 0, s[22:23]
	s_waitcnt vmcnt(21)
	v_pk_mul_f32 v[56:57], v[182:183], s[18:19] op_sel_hi:[1,0]
	s_waitcnt vmcnt(20)
	v_pk_mul_f32 v[62:63], v[188:189], s[18:19] op_sel_hi:[1,0]
	v_pk_mul_f32 v[60:61], v[186:187], s[18:19] op_sel_hi:[1,0]
	v_pk_mul_f32 v[58:59], v[184:185], s[18:19] op_sel_hi:[1,0]
	v_pk_fma_f32 v[52:53], v[52:53], v[124:125], v[56:57]
	v_pk_fma_f32 v[56:57], v[50:51], v[122:123], v[62:63]
	v_pk_fma_f32 v[50:51], v[48:49], v[120:121], v[60:61]
	v_pk_fma_f32 v[54:55], v[54:55], v[126:127], v[58:59]
	v_cvt_pk_bf16_f32 v48, v52, v53
	s_nop 0
	v_cvt_pk_bf16_f32 v49, v54, v55
	v_cvt_pk_bf16_f32 v50, v50, v51
	v_cvt_pk_bf16_f32 v51, v56, v57
	global_store_dwordx4 v[72:73], v[48:51], off offset:256 sc1
	s_nop 1
	v_lshl_add_u64 v[56:57], v[64:65], 1, s[64:65]
	s_waitcnt vmcnt(19)
	v_pk_mul_f32 v[48:49], v[190:191], s[18:19] op_sel_hi:[1,0]
	s_waitcnt vmcnt(18)
	v_pk_mul_f32 v[54:55], v[196:197], s[18:19] op_sel_hi:[1,0]
	v_pk_mul_f32 v[52:53], v[194:195], s[18:19] op_sel_hi:[1,0]
	v_pk_mul_f32 v[50:51], v[192:193], s[18:19] op_sel_hi:[1,0]
	v_pk_fma_f32 v[44:45], v[44:45], v[132:133], v[48:49]
	v_pk_fma_f32 v[48:49], v[42:43], v[130:131], v[54:55]
	v_pk_fma_f32 v[42:43], v[40:41], v[128:129], v[52:53]
	v_pk_fma_f32 v[46:47], v[46:47], v[134:135], v[50:51]
	v_cvt_pk_bf16_f32 v40, v44, v45
	s_nop 0
	v_cvt_pk_bf16_f32 v41, v46, v47
	v_cvt_pk_bf16_f32 v42, v42, v43
	v_cvt_pk_bf16_f32 v43, v48, v49
	global_store_dwordx4 v[56:57], v[40:43], off sc1
	s_nop 1
	v_lshl_add_u64 v[48:49], v[160:161], 0, s[24:25]
	s_waitcnt vmcnt(17)
	v_pk_mul_f32 v[40:41], v[198:199], s[18:19] op_sel_hi:[1,0]
	s_waitcnt vmcnt(16)
	v_pk_mul_f32 v[46:47], v[204:205], s[18:19] op_sel_hi:[1,0]
	v_pk_mul_f32 v[44:45], v[202:203], s[18:19] op_sel_hi:[1,0]
	v_pk_mul_f32 v[42:43], v[200:201], s[18:19] op_sel_hi:[1,0]
	v_pk_fma_f32 v[36:37], v[36:37], v[124:125], v[40:41]
	v_pk_fma_f32 v[40:41], v[34:35], v[122:123], v[46:47]
	v_pk_fma_f32 v[34:35], v[32:33], v[120:121], v[44:45]
	v_pk_fma_f32 v[38:39], v[38:39], v[126:127], v[42:43]
	v_cvt_pk_bf16_f32 v32, v36, v37
	s_nop 0
	v_cvt_pk_bf16_f32 v33, v38, v39
	v_cvt_pk_bf16_f32 v34, v34, v35
	v_cvt_pk_bf16_f32 v35, v40, v41
	global_store_dwordx4 v[56:57], v[32:35], off offset:256 sc1
	s_nop 1
	v_lshl_add_u64 v[40:41], v[48:49], 1, s[64:65]
	s_waitcnt vmcnt(15)
	v_pk_mul_f32 v[32:33], v[206:207], s[18:19] op_sel_hi:[1,0]
	s_waitcnt vmcnt(14)
	v_pk_mul_f32 v[38:39], v[212:213], s[18:19] op_sel_hi:[1,0]
	v_pk_mul_f32 v[36:37], v[210:211], s[18:19] op_sel_hi:[1,0]
	v_pk_mul_f32 v[34:35], v[208:209], s[18:19] op_sel_hi:[1,0]
	v_pk_fma_f32 v[28:29], v[28:29], v[132:133], v[32:33]
	v_pk_fma_f32 v[32:33], v[26:27], v[130:131], v[38:39]
	v_pk_fma_f32 v[26:27], v[24:25], v[128:129], v[36:37]
	v_pk_fma_f32 v[30:31], v[30:31], v[134:135], v[34:35]
	v_cvt_pk_bf16_f32 v24, v28, v29
	s_nop 0
	v_cvt_pk_bf16_f32 v25, v30, v31
	v_cvt_pk_bf16_f32 v26, v26, v27
	v_cvt_pk_bf16_f32 v27, v32, v33
	global_store_dwordx4 v[40:41], v[24:27], off sc1
	s_nop 1
	v_lshl_add_u64 v[32:33], v[160:161], 0, s[26:27]
	s_waitcnt vmcnt(13)
	v_pk_mul_f32 v[24:25], v[214:215], s[18:19] op_sel_hi:[1,0]
	s_waitcnt vmcnt(12)
	v_pk_mul_f32 v[30:31], v[220:221], s[18:19] op_sel_hi:[1,0]
	v_pk_mul_f32 v[28:29], v[218:219], s[18:19] op_sel_hi:[1,0]
	v_pk_mul_f32 v[26:27], v[216:217], s[18:19] op_sel_hi:[1,0]
	v_pk_fma_f32 v[20:21], v[20:21], v[124:125], v[24:25]
	v_pk_fma_f32 v[24:25], v[18:19], v[122:123], v[30:31]
	v_pk_fma_f32 v[18:19], v[16:17], v[120:121], v[28:29]
	v_pk_fma_f32 v[22:23], v[22:23], v[126:127], v[26:27]
	v_cvt_pk_bf16_f32 v16, v20, v21
	s_nop 0
	v_cvt_pk_bf16_f32 v17, v22, v23
	v_cvt_pk_bf16_f32 v18, v18, v19
	v_cvt_pk_bf16_f32 v19, v24, v25
	global_store_dwordx4 v[40:41], v[16:19], off offset:256 sc1
	s_nop 1
	v_lshl_add_u64 v[24:25], v[32:33], 1, s[64:65]
	s_waitcnt vmcnt(11)
	v_pk_mul_f32 v[16:17], v[222:223], s[18:19] op_sel_hi:[1,0]
	s_waitcnt vmcnt(10)
	v_pk_mul_f32 v[22:23], v[228:229], s[18:19] op_sel_hi:[1,0]
	v_pk_mul_f32 v[20:21], v[226:227], s[18:19] op_sel_hi:[1,0]
	v_pk_mul_f32 v[18:19], v[224:225], s[18:19] op_sel_hi:[1,0]
	v_pk_fma_f32 v[12:13], v[12:13], v[132:133], v[16:17]
	v_pk_fma_f32 v[16:17], v[10:11], v[130:131], v[22:23]
	v_pk_fma_f32 v[10:11], v[8:9], v[128:129], v[20:21]
	v_pk_fma_f32 v[14:15], v[14:15], v[134:135], v[18:19]
	v_cvt_pk_bf16_f32 v8, v12, v13
	s_nop 0
	v_cvt_pk_bf16_f32 v9, v14, v15
	v_cvt_pk_bf16_f32 v10, v10, v11
	v_cvt_pk_bf16_f32 v11, v16, v17
	global_store_dwordx4 v[24:25], v[8:11], off sc1
	s_nop 1
	s_waitcnt vmcnt(9)
	v_pk_mul_f32 v[8:9], v[230:231], s[18:19] op_sel_hi:[1,0]
	s_waitcnt vmcnt(8)
	v_pk_mul_f32 v[14:15], v[236:237], s[18:19] op_sel_hi:[1,0]
	v_pk_mul_f32 v[12:13], v[234:235], s[18:19] op_sel_hi:[1,0]
	v_pk_mul_f32 v[10:11], v[232:233], s[18:19] op_sel_hi:[1,0]
	v_pk_fma_f32 v[4:5], v[4:5], v[124:125], v[8:9]
	v_pk_fma_f32 v[8:9], v[2:3], v[122:123], v[14:15]
	v_pk_fma_f32 v[2:3], v[0:1], v[120:121], v[12:13]
	v_pk_fma_f32 v[6:7], v[6:7], v[126:127], v[10:11]
	v_cvt_pk_bf16_f32 v0, v4, v5
	s_nop 0
	v_cvt_pk_bf16_f32 v1, v6, v7
	v_cvt_pk_bf16_f32 v2, v2, v3
	v_cvt_pk_bf16_f32 v3, v8, v9
	global_store_dwordx4 v[24:25], v[0:3], off offset:256 sc1
	s_nop 1
	s_cbranch_vccnz .LBB0_333
	s_andn2_b64 vcc, exec, s[10:11]
	s_cbranch_vccnz .LBB0_332
	s_barrier
	s_branch .LBB0_332

.LBB0_574:
	v_mbcnt_lo_u32_b32 v132, -1, 0
	v_mbcnt_hi_u32_b32 v132, -1, v132
	global_load_dword v136, v148, s[8:9]
	s_lshl_b32 s24, s60, 8
	v_ashrrev_i32_e32 v133, 1, v132
	s_or_b32 s24, s24, s47
	v_and_b32_e32 v133, -8, v133
	v_add_u32_e32 v140, s24, v133
	s_lshl_b32 s24, s59, 8
	s_add_i32 s24, s24, s46
	v_and_or_b32 v142, v132, 15, s24
	v_ashrrev_i32_e32 v143, 31, v142
	v_ashrrev_i32_e32 v141, 31, v140
	v_lshlrev_b64 v[132:133], 11, v[142:143]
	v_lshl_add_u64 v[132:133], v[132:133], 0, v[140:141]
	v_lshlrev_b64 v[138:139], 1, v[132:133]
	v_lshl_add_u64 v[150:151], s[76:77], 0, v[138:139]
	global_load_dwordx4 v[132:135], v[150:151], off
	global_load_dwordx4 v[164:167], v[150:151], off offset:256
	s_mov_b64 s[98:99], 0x10000
	v_lshl_add_u64 v[224:225], v[150:151], 0, s[98:99]
	global_load_dwordx4 v[168:171], v[224:225], off
	global_load_dwordx4 v[172:175], v[224:225], off offset:256
	v_lshl_add_u64 v[224:225], v[224:225], 0, s[98:99]
	global_load_dwordx4 v[176:179], v[224:225], off
	global_load_dwordx4 v[180:183], v[224:225], off offset:256
	v_lshl_add_u64 v[224:225], v[224:225], 0, s[98:99]
	global_load_dwordx4 v[184:187], v[224:225], off
	global_load_dwordx4 v[188:191], v[224:225], off offset:256
	v_lshl_add_u64 v[224:225], v[150:151], 0, s[14:15]
	global_load_dwordx4 v[192:195], v[224:225], off
	global_load_dwordx4 v[196:199], v[224:225], off offset:256
	v_lshl_add_u64 v[224:225], v[150:151], 0, s[16:17]
	global_load_dwordx4 v[200:203], v[224:225], off
	global_load_dwordx4 v[204:207], v[224:225], off offset:256
	v_lshl_add_u64 v[224:225], v[150:151], 0, s[18:19]
	global_load_dwordx4 v[208:211], v[224:225], off
	global_load_dwordx4 v[212:215], v[224:225], off offset:256
	v_lshl_add_u64 v[224:225], v[150:151], 0, s[6:7]
	global_load_dwordx4 v[216:219], v[224:225], off
	global_load_dwordx4 v[220:223], v[224:225], off offset:256
	v_lshl_add_u64 v[152:153], s[64:65], 0, v[138:139]
	s_waitcnt vmcnt(16)
	v_div_scale_f32 v143, s[24:25], v136, v136, 1.0
	v_rcp_f32_e32 v149, v143
	v_div_scale_f32 v158, vcc, 1.0, v136, 1.0
	v_fma_f32 v154, -v143, v149, 1.0
	v_fmac_f32_e32 v149, v154, v149
	v_mul_f32_e32 v159, v158, v149
	v_fma_f32 v160, -v143, v159, v158
	v_fmac_f32_e32 v159, v160, v149
	v_fma_f32 v143, -v143, v159, v158
	v_div_fmas_f32 v143, v143, v149, v159
	v_div_fixup_f32 v136, v143, v136, 1.0
	s_andn2_b64 vcc, exec, s[0:1]
	s_waitcnt vmcnt(15)
	v_lshlrev_b32_e32 v154, 16, v132
	v_and_b32_e32 v155, 0xffff0000, v132
	v_lshlrev_b32_e32 v132, 16, v133
	v_and_b32_e32 v133, 0xffff0000, v133
	v_lshlrev_b32_e32 v156, 16, v134
	v_and_b32_e32 v157, 0xffff0000, v134
	v_lshlrev_b32_e32 v134, 16, v135
	v_and_b32_e32 v135, 0xffff0000, v135
	v_pk_mul_f32 v[132:133], v[132:133], s[12:13] op_sel_hi:[1,0]
	v_pk_mul_f32 v[156:157], v[156:157], s[12:13] op_sel_hi:[1,0]
	v_pk_mul_f32 v[134:135], v[134:135], s[12:13] op_sel_hi:[1,0]
	v_pk_mul_f32 v[154:155], v[154:155], s[12:13] op_sel_hi:[1,0]
	v_pk_fma_f32 v[126:127], v[126:127], v[136:137], v[132:133] op_sel_hi:[1,0,1]
	v_pk_fma_f32 v[132:133], v[122:123], v[136:137], v[134:135] op_sel_hi:[1,0,1]
	v_pk_fma_f32 v[122:123], v[120:121], v[136:137], v[156:157] op_sel_hi:[1,0,1]
	v_pk_fma_f32 v[124:125], v[124:125], v[136:137], v[154:155] op_sel_hi:[1,0,1]
	s_mov_b64 s[0:1], -1
	v_cvt_pk_bf16_f32 v120, v124, v125
	v_cvt_pk_bf16_f32 v121, v126, v127
	v_cvt_pk_bf16_f32 v122, v122, v123
	v_cvt_pk_bf16_f32 v123, v132, v133
	global_store_dwordx4 v[152:153], v[120:123], off sc1
	v_or_b32_e32 v124, 16, v142
	v_ashrrev_i32_e32 v125, 31, v124
	v_lshlrev_b64 v[124:125], 11, v[124:125]
	v_lshl_add_u64 v[124:125], v[124:125], 0, v[140:141]
	v_lshlrev_b64 v[124:125], 1, v[124:125]
	s_waitcnt vmcnt(15)
	v_lshlrev_b32_e32 v132, 16, v164
	v_and_b32_e32 v133, 0xffff0000, v164
	v_lshlrev_b32_e32 v120, 16, v165
	v_and_b32_e32 v121, 0xffff0000, v165
	v_lshlrev_b32_e32 v134, 16, v166
	v_and_b32_e32 v135, 0xffff0000, v166
	v_lshlrev_b32_e32 v122, 16, v167
	v_and_b32_e32 v123, 0xffff0000, v167
	v_pk_mul_f32 v[120:121], v[120:121], s[12:13] op_sel_hi:[1,0]
	v_pk_mul_f32 v[134:135], v[134:135], s[12:13] op_sel_hi:[1,0]
	v_pk_mul_f32 v[122:123], v[122:123], s[12:13] op_sel_hi:[1,0]
	v_pk_mul_f32 v[132:133], v[132:133], s[12:13] op_sel_hi:[1,0]
	v_pk_fma_f32 v[118:119], v[118:119], v[136:137], v[120:121] op_sel_hi:[1,0,1]
	v_pk_fma_f32 v[120:121], v[114:115], v[136:137], v[122:123] op_sel_hi:[1,0,1]
	v_pk_fma_f32 v[114:115], v[112:113], v[136:137], v[134:135] op_sel_hi:[1,0,1]
	v_pk_fma_f32 v[116:117], v[116:117], v[136:137], v[132:133] op_sel_hi:[1,0,1]
	s_nop 0
	v_cvt_pk_bf16_f32 v112, v116, v117
	v_cvt_pk_bf16_f32 v113, v118, v119
	v_cvt_pk_bf16_f32 v114, v114, v115
	v_cvt_pk_bf16_f32 v115, v120, v121
	global_store_dwordx4 v[152:153], v[112:115], off offset:256 sc1
	v_lshl_add_u64 v[116:117], s[64:65], 0, v[124:125]
	s_waitcnt vmcnt(15)
	v_lshlrev_b32_e32 v118, 16, v168
	v_and_b32_e32 v119, 0xffff0000, v168
	v_lshlrev_b32_e32 v112, 16, v169
	v_and_b32_e32 v113, 0xffff0000, v169
	v_lshlrev_b32_e32 v120, 16, v170
	v_and_b32_e32 v121, 0xffff0000, v170
	v_lshlrev_b32_e32 v114, 16, v171
	v_and_b32_e32 v115, 0xffff0000, v171
	v_pk_mul_f32 v[112:113], v[112:113], s[12:13] op_sel_hi:[1,0]
	v_pk_mul_f32 v[120:121], v[120:121], s[12:13] op_sel_hi:[1,0]
	v_pk_mul_f32 v[114:115], v[114:115], s[12:13] op_sel_hi:[1,0]
	v_pk_mul_f32 v[118:119], v[118:119], s[12:13] op_sel_hi:[1,0]
	v_pk_fma_f32 v[110:111], v[110:111], v[136:137], v[112:113] op_sel_hi:[1,0,1]
	v_pk_fma_f32 v[112:113], v[106:107], v[136:137], v[114:115] op_sel_hi:[1,0,1]
	v_pk_fma_f32 v[106:107], v[104:105], v[136:137], v[120:121] op_sel_hi:[1,0,1]
	v_pk_fma_f32 v[108:109], v[108:109], v[136:137], v[118:119] op_sel_hi:[1,0,1]
	s_nop 0
	v_cvt_pk_bf16_f32 v104, v108, v109
	v_cvt_pk_bf16_f32 v105, v110, v111
	v_cvt_pk_bf16_f32 v106, v106, v107
	v_cvt_pk_bf16_f32 v107, v112, v113
	global_store_dwordx4 v[116:117], v[104:107], off sc1
	v_or_b32_e32 v108, 32, v142
	v_ashrrev_i32_e32 v109, 31, v108
	v_lshlrev_b64 v[108:109], 11, v[108:109]
	v_lshl_add_u64 v[108:109], v[108:109], 0, v[140:141]
	v_lshlrev_b64 v[108:109], 1, v[108:109]
	s_waitcnt vmcnt(15)
	v_lshlrev_b32_e32 v112, 16, v172
	v_and_b32_e32 v113, 0xffff0000, v172
	v_lshlrev_b32_e32 v104, 16, v173
	v_and_b32_e32 v105, 0xffff0000, v173
	v_lshlrev_b32_e32 v114, 16, v174
	v_and_b32_e32 v115, 0xffff0000, v174
	v_lshlrev_b32_e32 v106, 16, v175
	v_and_b32_e32 v107, 0xffff0000, v175
	v_pk_mul_f32 v[104:105], v[104:105], s[12:13] op_sel_hi:[1,0]
	v_pk_mul_f32 v[114:115], v[114:115], s[12:13] op_sel_hi:[1,0]
	v_pk_mul_f32 v[106:107], v[106:107], s[12:13] op_sel_hi:[1,0]
	v_pk_mul_f32 v[112:113], v[112:113], s[12:13] op_sel_hi:[1,0]
	v_pk_fma_f32 v[102:103], v[102:103], v[136:137], v[104:105] op_sel_hi:[1,0,1]
	v_pk_fma_f32 v[104:105], v[98:99], v[136:137], v[106:107] op_sel_hi:[1,0,1]
	v_pk_fma_f32 v[98:99], v[96:97], v[136:137], v[114:115] op_sel_hi:[1,0,1]
	v_pk_fma_f32 v[100:101], v[100:101], v[136:137], v[112:113] op_sel_hi:[1,0,1]
	s_nop 0
	v_cvt_pk_bf16_f32 v96, v100, v101
	v_cvt_pk_bf16_f32 v97, v102, v103
	v_cvt_pk_bf16_f32 v98, v98, v99
	v_cvt_pk_bf16_f32 v99, v104, v105
	global_store_dwordx4 v[116:117], v[96:99], off offset:256 sc1
	v_lshl_add_u64 v[100:101], s[64:65], 0, v[108:109]
	s_waitcnt vmcnt(15)
	v_lshlrev_b32_e32 v102, 16, v176
	v_and_b32_e32 v103, 0xffff0000, v176
	v_lshlrev_b32_e32 v96, 16, v177
	v_and_b32_e32 v97, 0xffff0000, v177
	v_lshlrev_b32_e32 v104, 16, v178
	v_and_b32_e32 v105, 0xffff0000, v178
	v_lshlrev_b32_e32 v98, 16, v179
	v_and_b32_e32 v99, 0xffff0000, v179
	v_pk_mul_f32 v[96:97], v[96:97], s[12:13] op_sel_hi:[1,0]
	v_pk_mul_f32 v[104:105], v[104:105], s[12:13] op_sel_hi:[1,0]
	v_pk_mul_f32 v[98:99], v[98:99], s[12:13] op_sel_hi:[1,0]
	v_pk_mul_f32 v[102:103], v[102:103], s[12:13] op_sel_hi:[1,0]
	v_pk_fma_f32 v[94:95], v[94:95], v[136:137], v[96:97] op_sel_hi:[1,0,1]
	v_pk_fma_f32 v[96:97], v[90:91], v[136:137], v[98:99] op_sel_hi:[1,0,1]
	v_pk_fma_f32 v[90:91], v[88:89], v[136:137], v[104:105] op_sel_hi:[1,0,1]
	v_pk_fma_f32 v[92:93], v[92:93], v[136:137], v[102:103] op_sel_hi:[1,0,1]
	s_nop 0
	v_cvt_pk_bf16_f32 v88, v92, v93
	v_cvt_pk_bf16_f32 v89, v94, v95
	v_cvt_pk_bf16_f32 v90, v90, v91
	v_cvt_pk_bf16_f32 v91, v96, v97
	global_store_dwordx4 v[100:101], v[88:91], off sc1
	v_or_b32_e32 v92, 48, v142
	v_ashrrev_i32_e32 v93, 31, v92
	v_lshlrev_b64 v[92:93], 11, v[92:93]
	v_lshl_add_u64 v[92:93], v[92:93], 0, v[140:141]
	v_lshlrev_b64 v[92:93], 1, v[92:93]
	s_waitcnt vmcnt(15)
	v_lshlrev_b32_e32 v96, 16, v180
	v_and_b32_e32 v97, 0xffff0000, v180
	v_lshlrev_b32_e32 v88, 16, v181
	v_and_b32_e32 v89, 0xffff0000, v181
	v_lshlrev_b32_e32 v98, 16, v182
	v_and_b32_e32 v99, 0xffff0000, v182
	v_lshlrev_b32_e32 v90, 16, v183
	v_and_b32_e32 v91, 0xffff0000, v183
	v_pk_mul_f32 v[88:89], v[88:89], s[12:13] op_sel_hi:[1,0]
	v_pk_mul_f32 v[98:99], v[98:99], s[12:13] op_sel_hi:[1,0]
	v_pk_mul_f32 v[90:91], v[90:91], s[12:13] op_sel_hi:[1,0]
	v_pk_mul_f32 v[96:97], v[96:97], s[12:13] op_sel_hi:[1,0]
	v_pk_fma_f32 v[86:87], v[86:87], v[136:137], v[88:89] op_sel_hi:[1,0,1]
	v_pk_fma_f32 v[88:89], v[82:83], v[136:137], v[90:91] op_sel_hi:[1,0,1]
	v_pk_fma_f32 v[82:83], v[80:81], v[136:137], v[98:99] op_sel_hi:[1,0,1]
	v_pk_fma_f32 v[84:85], v[84:85], v[136:137], v[96:97] op_sel_hi:[1,0,1]
	s_nop 0
	v_cvt_pk_bf16_f32 v80, v84, v85
	v_cvt_pk_bf16_f32 v81, v86, v87
	v_cvt_pk_bf16_f32 v82, v82, v83
	v_cvt_pk_bf16_f32 v83, v88, v89
	global_store_dwordx4 v[100:101], v[80:83], off offset:256 sc1
	v_lshl_add_u64 v[84:85], s[64:65], 0, v[92:93]
	s_waitcnt vmcnt(15)
	v_lshlrev_b32_e32 v86, 16, v184
	v_and_b32_e32 v87, 0xffff0000, v184
	v_lshlrev_b32_e32 v80, 16, v185
	v_and_b32_e32 v81, 0xffff0000, v185
	v_lshlrev_b32_e32 v88, 16, v186
	v_and_b32_e32 v89, 0xffff0000, v186
	v_lshlrev_b32_e32 v82, 16, v187
	v_and_b32_e32 v83, 0xffff0000, v187
	v_pk_mul_f32 v[80:81], v[80:81], s[12:13] op_sel_hi:[1,0]
	v_pk_mul_f32 v[88:89], v[88:89], s[12:13] op_sel_hi:[1,0]
	v_pk_mul_f32 v[82:83], v[82:83], s[12:13] op_sel_hi:[1,0]
	v_pk_mul_f32 v[86:87], v[86:87], s[12:13] op_sel_hi:[1,0]
	v_pk_fma_f32 v[78:79], v[78:79], v[136:137], v[80:81] op_sel_hi:[1,0,1]
	v_pk_fma_f32 v[80:81], v[74:75], v[136:137], v[82:83] op_sel_hi:[1,0,1]
	v_pk_fma_f32 v[74:75], v[72:73], v[136:137], v[88:89] op_sel_hi:[1,0,1]
	v_pk_fma_f32 v[76:77], v[76:77], v[136:137], v[86:87] op_sel_hi:[1,0,1]
	s_nop 0
	v_cvt_pk_bf16_f32 v72, v76, v77
	v_cvt_pk_bf16_f32 v73, v78, v79
	v_cvt_pk_bf16_f32 v74, v74, v75
	v_cvt_pk_bf16_f32 v75, v80, v81
	global_store_dwordx4 v[84:85], v[72:75], off sc1
	v_lshl_add_u64 v[76:77], v[138:139], 0, s[14:15]
	s_waitcnt vmcnt(15)
	v_lshlrev_b32_e32 v80, 16, v188
	v_and_b32_e32 v81, 0xffff0000, v188
	v_lshlrev_b32_e32 v72, 16, v189
	v_and_b32_e32 v73, 0xffff0000, v189
	v_lshlrev_b32_e32 v82, 16, v190
	v_and_b32_e32 v83, 0xffff0000, v190
	v_lshlrev_b32_e32 v74, 16, v191
	v_and_b32_e32 v75, 0xffff0000, v191
	v_pk_mul_f32 v[72:73], v[72:73], s[12:13] op_sel_hi:[1,0]
	v_pk_mul_f32 v[82:83], v[82:83], s[12:13] op_sel_hi:[1,0]
	v_pk_mul_f32 v[74:75], v[74:75], s[12:13] op_sel_hi:[1,0]
	v_pk_mul_f32 v[80:81], v[80:81], s[12:13] op_sel_hi:[1,0]
	v_pk_fma_f32 v[70:71], v[70:71], v[136:137], v[72:73] op_sel_hi:[1,0,1]
	v_pk_fma_f32 v[72:73], v[66:67], v[136:137], v[74:75] op_sel_hi:[1,0,1]
	v_pk_fma_f32 v[66:67], v[64:65], v[136:137], v[82:83] op_sel_hi:[1,0,1]
	v_pk_fma_f32 v[68:69], v[68:69], v[136:137], v[80:81] op_sel_hi:[1,0,1]
	s_nop 0
	v_cvt_pk_bf16_f32 v64, v68, v69
	v_cvt_pk_bf16_f32 v65, v70, v71
	v_cvt_pk_bf16_f32 v66, v66, v67
	v_cvt_pk_bf16_f32 v67, v72, v73
	global_store_dwordx4 v[84:85], v[64:67], off offset:256 sc1
	v_lshl_add_u64 v[68:69], s[64:65], 0, v[76:77]
	s_waitcnt vmcnt(15)
	v_lshlrev_b32_e32 v70, 16, v192
	v_and_b32_e32 v71, 0xffff0000, v192
	v_lshlrev_b32_e32 v64, 16, v193
	v_and_b32_e32 v65, 0xffff0000, v193
	v_lshlrev_b32_e32 v72, 16, v194
	v_and_b32_e32 v73, 0xffff0000, v194
	v_lshlrev_b32_e32 v66, 16, v195
	v_and_b32_e32 v67, 0xffff0000, v195
	v_pk_mul_f32 v[64:65], v[64:65], s[12:13] op_sel_hi:[1,0]
	v_pk_mul_f32 v[72:73], v[72:73], s[12:13] op_sel_hi:[1,0]
	v_pk_mul_f32 v[66:67], v[66:67], s[12:13] op_sel_hi:[1,0]
	v_pk_mul_f32 v[70:71], v[70:71], s[12:13] op_sel_hi:[1,0]
	v_pk_fma_f32 v[62:63], v[62:63], v[136:137], v[64:65] op_sel_hi:[1,0,1]
	v_pk_fma_f32 v[64:65], v[58:59], v[136:137], v[66:67] op_sel_hi:[1,0,1]
	v_pk_fma_f32 v[58:59], v[56:57], v[136:137], v[72:73] op_sel_hi:[1,0,1]
	v_pk_fma_f32 v[60:61], v[60:61], v[136:137], v[70:71] op_sel_hi:[1,0,1]
	s_nop 0
	v_cvt_pk_bf16_f32 v56, v60, v61
	v_cvt_pk_bf16_f32 v57, v62, v63
	v_cvt_pk_bf16_f32 v58, v58, v59
	v_cvt_pk_bf16_f32 v59, v64, v65
	global_store_dwordx4 v[68:69], v[56:59], off sc1
	v_lshl_add_u64 v[60:61], v[138:139], 0, s[16:17]
	s_waitcnt vmcnt(15)
	v_lshlrev_b32_e32 v64, 16, v196
	v_and_b32_e32 v65, 0xffff0000, v196
	v_lshlrev_b32_e32 v56, 16, v197
	v_and_b32_e32 v57, 0xffff0000, v197
	v_lshlrev_b32_e32 v66, 16, v198
	v_and_b32_e32 v67, 0xffff0000, v198
	v_lshlrev_b32_e32 v58, 16, v199
	v_and_b32_e32 v59, 0xffff0000, v199
	v_pk_mul_f32 v[56:57], v[56:57], s[12:13] op_sel_hi:[1,0]
	v_pk_mul_f32 v[66:67], v[66:67], s[12:13] op_sel_hi:[1,0]
	v_pk_mul_f32 v[58:59], v[58:59], s[12:13] op_sel_hi:[1,0]
	v_pk_mul_f32 v[64:65], v[64:65], s[12:13] op_sel_hi:[1,0]
	v_pk_fma_f32 v[54:55], v[54:55], v[136:137], v[56:57] op_sel_hi:[1,0,1]
	v_pk_fma_f32 v[56:57], v[50:51], v[136:137], v[58:59] op_sel_hi:[1,0,1]
	v_pk_fma_f32 v[50:51], v[48:49], v[136:137], v[66:67] op_sel_hi:[1,0,1]
	v_pk_fma_f32 v[52:53], v[52:53], v[136:137], v[64:65] op_sel_hi:[1,0,1]
	s_nop 0
	v_cvt_pk_bf16_f32 v48, v52, v53
	v_cvt_pk_bf16_f32 v49, v54, v55
	v_cvt_pk_bf16_f32 v50, v50, v51
	v_cvt_pk_bf16_f32 v51, v56, v57
	global_store_dwordx4 v[68:69], v[48:51], off offset:256 sc1
	v_lshl_add_u64 v[52:53], s[64:65], 0, v[60:61]
	s_waitcnt vmcnt(15)
	v_lshlrev_b32_e32 v54, 16, v200
	v_and_b32_e32 v55, 0xffff0000, v200
	v_lshlrev_b32_e32 v48, 16, v201
	v_and_b32_e32 v49, 0xffff0000, v201
	v_lshlrev_b32_e32 v56, 16, v202
	v_and_b32_e32 v57, 0xffff0000, v202
	v_lshlrev_b32_e32 v50, 16, v203
	v_and_b32_e32 v51, 0xffff0000, v203
	v_pk_mul_f32 v[48:49], v[48:49], s[12:13] op_sel_hi:[1,0]
	v_pk_mul_f32 v[56:57], v[56:57], s[12:13] op_sel_hi:[1,0]
	v_pk_mul_f32 v[50:51], v[50:51], s[12:13] op_sel_hi:[1,0]
	v_pk_mul_f32 v[54:55], v[54:55], s[12:13] op_sel_hi:[1,0]
	v_pk_fma_f32 v[46:47], v[46:47], v[136:137], v[48:49] op_sel_hi:[1,0,1]
	v_pk_fma_f32 v[48:49], v[42:43], v[136:137], v[50:51] op_sel_hi:[1,0,1]
	v_pk_fma_f32 v[42:43], v[40:41], v[136:137], v[56:57] op_sel_hi:[1,0,1]
	v_pk_fma_f32 v[44:45], v[44:45], v[136:137], v[54:55] op_sel_hi:[1,0,1]
	s_nop 0
	v_cvt_pk_bf16_f32 v40, v44, v45
	v_cvt_pk_bf16_f32 v41, v46, v47
	v_cvt_pk_bf16_f32 v42, v42, v43
	v_cvt_pk_bf16_f32 v43, v48, v49
	global_store_dwordx4 v[52:53], v[40:43], off sc1
	v_lshl_add_u64 v[44:45], v[138:139], 0, s[18:19]
	s_waitcnt vmcnt(15)
	v_lshlrev_b32_e32 v48, 16, v204
	v_and_b32_e32 v49, 0xffff0000, v204
	v_lshlrev_b32_e32 v40, 16, v205
	v_and_b32_e32 v41, 0xffff0000, v205
	v_lshlrev_b32_e32 v50, 16, v206
	v_and_b32_e32 v51, 0xffff0000, v206
	v_lshlrev_b32_e32 v42, 16, v207
	v_and_b32_e32 v43, 0xffff0000, v207
	v_pk_mul_f32 v[40:41], v[40:41], s[12:13] op_sel_hi:[1,0]
	v_pk_mul_f32 v[50:51], v[50:51], s[12:13] op_sel_hi:[1,0]
	v_pk_mul_f32 v[42:43], v[42:43], s[12:13] op_sel_hi:[1,0]
	v_pk_mul_f32 v[48:49], v[48:49], s[12:13] op_sel_hi:[1,0]
	v_pk_fma_f32 v[38:39], v[38:39], v[136:137], v[40:41] op_sel_hi:[1,0,1]
	v_pk_fma_f32 v[40:41], v[34:35], v[136:137], v[42:43] op_sel_hi:[1,0,1]
	v_pk_fma_f32 v[34:35], v[32:33], v[136:137], v[50:51] op_sel_hi:[1,0,1]
	v_pk_fma_f32 v[36:37], v[36:37], v[136:137], v[48:49] op_sel_hi:[1,0,1]
	s_nop 0
	v_cvt_pk_bf16_f32 v32, v36, v37
	v_cvt_pk_bf16_f32 v33, v38, v39
	v_cvt_pk_bf16_f32 v34, v34, v35
	v_cvt_pk_bf16_f32 v35, v40, v41
	global_store_dwordx4 v[52:53], v[32:35], off offset:256 sc1
	v_lshl_add_u64 v[36:37], s[64:65], 0, v[44:45]
	s_waitcnt vmcnt(15)
	v_lshlrev_b32_e32 v38, 16, v208
	v_and_b32_e32 v39, 0xffff0000, v208
	v_lshlrev_b32_e32 v32, 16, v209
	v_and_b32_e32 v33, 0xffff0000, v209
	v_lshlrev_b32_e32 v40, 16, v210
	v_and_b32_e32 v41, 0xffff0000, v210
	v_lshlrev_b32_e32 v34, 16, v211
	v_and_b32_e32 v35, 0xffff0000, v211
	v_pk_mul_f32 v[32:33], v[32:33], s[12:13] op_sel_hi:[1,0]
	v_pk_mul_f32 v[40:41], v[40:41], s[12:13] op_sel_hi:[1,0]
	v_pk_mul_f32 v[34:35], v[34:35], s[12:13] op_sel_hi:[1,0]
	v_pk_mul_f32 v[38:39], v[38:39], s[12:13] op_sel_hi:[1,0]
	v_pk_fma_f32 v[30:31], v[30:31], v[136:137], v[32:33] op_sel_hi:[1,0,1]
	v_pk_fma_f32 v[32:33], v[26:27], v[136:137], v[34:35] op_sel_hi:[1,0,1]
	v_pk_fma_f32 v[26:27], v[24:25], v[136:137], v[40:41] op_sel_hi:[1,0,1]
	v_pk_fma_f32 v[28:29], v[28:29], v[136:137], v[38:39] op_sel_hi:[1,0,1]
	s_nop 0
	v_cvt_pk_bf16_f32 v24, v28, v29
	v_cvt_pk_bf16_f32 v25, v30, v31
	v_cvt_pk_bf16_f32 v26, v26, v27
	v_cvt_pk_bf16_f32 v27, v32, v33
	global_store_dwordx4 v[36:37], v[24:27], off sc1
	v_lshl_add_u64 v[28:29], v[138:139], 0, s[6:7]
	s_waitcnt vmcnt(15)
	v_lshlrev_b32_e32 v32, 16, v212
	v_and_b32_e32 v33, 0xffff0000, v212
	v_lshlrev_b32_e32 v24, 16, v213
	v_and_b32_e32 v25, 0xffff0000, v213
	v_lshlrev_b32_e32 v34, 16, v214
	v_and_b32_e32 v35, 0xffff0000, v214
	v_lshlrev_b32_e32 v26, 16, v215
	v_and_b32_e32 v27, 0xffff0000, v215
	v_pk_mul_f32 v[24:25], v[24:25], s[12:13] op_sel_hi:[1,0]
	v_pk_mul_f32 v[34:35], v[34:35], s[12:13] op_sel_hi:[1,0]
	v_pk_mul_f32 v[26:27], v[26:27], s[12:13] op_sel_hi:[1,0]
	v_pk_mul_f32 v[32:33], v[32:33], s[12:13] op_sel_hi:[1,0]
	v_pk_fma_f32 v[22:23], v[22:23], v[136:137], v[24:25] op_sel_hi:[1,0,1]
	v_pk_fma_f32 v[24:25], v[18:19], v[136:137], v[26:27] op_sel_hi:[1,0,1]
	v_pk_fma_f32 v[18:19], v[16:17], v[136:137], v[34:35] op_sel_hi:[1,0,1]
	v_pk_fma_f32 v[20:21], v[20:21], v[136:137], v[32:33] op_sel_hi:[1,0,1]
	s_nop 0
	v_cvt_pk_bf16_f32 v16, v20, v21
	v_cvt_pk_bf16_f32 v17, v22, v23
	v_cvt_pk_bf16_f32 v18, v18, v19
	v_cvt_pk_bf16_f32 v19, v24, v25
	global_store_dwordx4 v[36:37], v[16:19], off offset:256 sc1
	v_lshl_add_u64 v[20:21], s[64:65], 0, v[28:29]
	s_waitcnt vmcnt(15)
	v_lshlrev_b32_e32 v22, 16, v216
	v_and_b32_e32 v23, 0xffff0000, v216
	v_lshlrev_b32_e32 v16, 16, v217
	v_and_b32_e32 v17, 0xffff0000, v217
	v_lshlrev_b32_e32 v24, 16, v218
	v_and_b32_e32 v25, 0xffff0000, v218
	v_lshlrev_b32_e32 v18, 16, v219
	v_and_b32_e32 v19, 0xffff0000, v219
	v_pk_mul_f32 v[16:17], v[16:17], s[12:13] op_sel_hi:[1,0]
	v_pk_mul_f32 v[24:25], v[24:25], s[12:13] op_sel_hi:[1,0]
	v_pk_mul_f32 v[18:19], v[18:19], s[12:13] op_sel_hi:[1,0]
	v_pk_mul_f32 v[22:23], v[22:23], s[12:13] op_sel_hi:[1,0]
	v_pk_fma_f32 v[14:15], v[14:15], v[136:137], v[16:17] op_sel_hi:[1,0,1]
	v_pk_fma_f32 v[16:17], v[10:11], v[136:137], v[18:19] op_sel_hi:[1,0,1]
	v_pk_fma_f32 v[10:11], v[8:9], v[136:137], v[24:25] op_sel_hi:[1,0,1]
	v_pk_fma_f32 v[12:13], v[12:13], v[136:137], v[22:23] op_sel_hi:[1,0,1]
	s_nop 0
	v_cvt_pk_bf16_f32 v8, v12, v13
	v_cvt_pk_bf16_f32 v9, v14, v15
	v_cvt_pk_bf16_f32 v10, v10, v11
	v_cvt_pk_bf16_f32 v11, v16, v17
	global_store_dwordx4 v[20:21], v[8:11], off sc1
	s_waitcnt vmcnt(15)
	v_lshlrev_b32_e32 v12, 16, v220
	v_and_b32_e32 v13, 0xffff0000, v220
	v_lshlrev_b32_e32 v8, 16, v221
	v_and_b32_e32 v9, 0xffff0000, v221
	v_lshlrev_b32_e32 v14, 16, v222
	v_and_b32_e32 v15, 0xffff0000, v222
	v_lshlrev_b32_e32 v10, 16, v223
	v_and_b32_e32 v11, 0xffff0000, v223
	v_pk_mul_f32 v[8:9], v[8:9], s[12:13] op_sel_hi:[1,0]
	v_pk_mul_f32 v[14:15], v[14:15], s[12:13] op_sel_hi:[1,0]
	v_pk_mul_f32 v[10:11], v[10:11], s[12:13] op_sel_hi:[1,0]
	v_pk_mul_f32 v[12:13], v[12:13], s[12:13] op_sel_hi:[1,0]
	v_pk_fma_f32 v[6:7], v[6:7], v[136:137], v[8:9] op_sel_hi:[1,0,1]
	v_pk_fma_f32 v[8:9], v[2:3], v[136:137], v[10:11] op_sel_hi:[1,0,1]
	v_pk_fma_f32 v[2:3], v[0:1], v[136:137], v[14:15] op_sel_hi:[1,0,1]
	v_pk_fma_f32 v[4:5], v[4:5], v[136:137], v[12:13] op_sel_hi:[1,0,1]
	s_nop 0
	v_cvt_pk_bf16_f32 v0, v4, v5
	v_cvt_pk_bf16_f32 v1, v6, v7
	v_cvt_pk_bf16_f32 v2, v2, v3
	v_cvt_pk_bf16_f32 v3, v8, v9
	global_store_dwordx4 v[20:21], v[0:3], off offset:256 sc1
	s_cbranch_vccnz .LBB0_563
	s_andn2_b64 vcc, exec, s[4:5]
	s_cbranch_vccnz .LBB0_562
	s_barrier
	s_branch .LBB0_562

.LBB0_1625:
	v_mbcnt_lo_u32_b32 v128, -1, 0
	v_mbcnt_hi_u32_b32 v128, -1, v128
	global_load_dword v132, v148, s[6:7]
	s_lshl_b32 s21, s30, 8
	v_ashrrev_i32_e32 v129, 1, v128
	s_or_b32 s21, s21, s53
	v_and_b32_e32 v129, -8, v129
	v_add_u32_e32 v136, s21, v129
	s_lshl_b32 s21, s28, 8
	s_add_i32 s21, s21, s52
	v_and_or_b32 v138, v128, 15, s21
	v_ashrrev_i32_e32 v139, 31, v138
	v_ashrrev_i32_e32 v137, 31, v136
	v_lshlrev_b64 v[128:129], 11, v[138:139]
	v_lshl_add_u64 v[128:129], v[128:129], 0, v[136:137]
	v_lshlrev_b64 v[134:135], 1, v[128:129]
	v_lshl_add_u64 v[150:151], s[76:77], 0, v[134:135]
	global_load_dwordx4 v[128:131], v[150:151], off
	global_load_dwordx4 v[164:167], v[150:151], off offset:256
	s_mov_b64 s[98:99], 0x10000
	v_lshl_add_u64 v[224:225], v[150:151], 0, s[98:99]
	global_load_dwordx4 v[168:171], v[224:225], off
	global_load_dwordx4 v[172:175], v[224:225], off offset:256
	v_lshl_add_u64 v[224:225], v[224:225], 0, s[98:99]
	global_load_dwordx4 v[176:179], v[224:225], off
	global_load_dwordx4 v[180:183], v[224:225], off offset:256
	v_lshl_add_u64 v[224:225], v[224:225], 0, s[98:99]
	global_load_dwordx4 v[184:187], v[224:225], off
	global_load_dwordx4 v[188:191], v[224:225], off offset:256
	v_lshl_add_u64 v[224:225], v[150:151], 0, s[12:13]
	global_load_dwordx4 v[192:195], v[224:225], off
	global_load_dwordx4 v[196:199], v[224:225], off offset:256
	v_lshl_add_u64 v[224:225], v[150:151], 0, s[14:15]
	global_load_dwordx4 v[200:203], v[224:225], off
	global_load_dwordx4 v[204:207], v[224:225], off offset:256
	v_lshl_add_u64 v[224:225], v[150:151], 0, s[16:17]
	global_load_dwordx4 v[208:211], v[224:225], off
	global_load_dwordx4 v[212:215], v[224:225], off offset:256
	v_lshl_add_u64 v[224:225], v[150:151], 0, s[18:19]
	global_load_dwordx4 v[216:219], v[224:225], off
	global_load_dwordx4 v[220:223], v[224:225], off offset:256
	v_lshl_add_u64 v[152:153], s[64:65], 0, v[134:135]
	s_waitcnt vmcnt(16)
	v_div_scale_f32 v139, s[34:35], v132, v132, 1.0
	v_rcp_f32_e32 v149, v139
	v_div_scale_f32 v158, vcc, 1.0, v132, 1.0
	v_fma_f32 v154, -v139, v149, 1.0
	v_fmac_f32_e32 v149, v154, v149
	v_mul_f32_e32 v159, v158, v149
	v_fma_f32 v160, -v139, v159, v158
	v_fmac_f32_e32 v159, v160, v149
	v_fma_f32 v139, -v139, v159, v158
	v_div_fmas_f32 v139, v139, v149, v159
	v_div_fixup_f32 v132, v139, v132, 1.0
	s_andn2_b64 vcc, exec, s[0:1]
	s_waitcnt vmcnt(15)
	v_lshlrev_b32_e32 v154, 16, v128
	v_and_b32_e32 v155, 0xffff0000, v128
	v_lshlrev_b32_e32 v128, 16, v129
	v_and_b32_e32 v129, 0xffff0000, v129
	v_lshlrev_b32_e32 v156, 16, v130
	v_and_b32_e32 v157, 0xffff0000, v130
	v_lshlrev_b32_e32 v130, 16, v131
	v_and_b32_e32 v131, 0xffff0000, v131
	v_pk_mul_f32 v[128:129], v[128:129], s[10:11] op_sel_hi:[1,0]
	v_pk_mul_f32 v[156:157], v[156:157], s[10:11] op_sel_hi:[1,0]
	v_pk_mul_f32 v[130:131], v[130:131], s[10:11] op_sel_hi:[1,0]
	v_pk_mul_f32 v[154:155], v[154:155], s[10:11] op_sel_hi:[1,0]
	v_pk_fma_f32 v[126:127], v[126:127], v[132:133], v[128:129] op_sel_hi:[1,0,1]
	v_pk_fma_f32 v[128:129], v[122:123], v[132:133], v[130:131] op_sel_hi:[1,0,1]
	v_pk_fma_f32 v[122:123], v[120:121], v[132:133], v[156:157] op_sel_hi:[1,0,1]
	v_pk_fma_f32 v[124:125], v[124:125], v[132:133], v[154:155] op_sel_hi:[1,0,1]
	s_mov_b64 s[0:1], -1
	v_cvt_pk_bf16_f32 v120, v124, v125
	v_cvt_pk_bf16_f32 v121, v126, v127
	v_cvt_pk_bf16_f32 v122, v122, v123
	v_cvt_pk_bf16_f32 v123, v128, v129
	global_store_dwordx4 v[152:153], v[120:123], off sc1
	v_or_b32_e32 v124, 16, v138
	v_ashrrev_i32_e32 v125, 31, v124
	v_lshlrev_b64 v[124:125], 11, v[124:125]
	v_lshl_add_u64 v[124:125], v[124:125], 0, v[136:137]
	v_lshlrev_b64 v[124:125], 1, v[124:125]
	s_waitcnt vmcnt(15)
	v_lshlrev_b32_e32 v128, 16, v164
	v_and_b32_e32 v129, 0xffff0000, v164
	v_lshlrev_b32_e32 v120, 16, v165
	v_and_b32_e32 v121, 0xffff0000, v165
	v_lshlrev_b32_e32 v130, 16, v166
	v_and_b32_e32 v131, 0xffff0000, v166
	v_lshlrev_b32_e32 v122, 16, v167
	v_and_b32_e32 v123, 0xffff0000, v167
	v_pk_mul_f32 v[120:121], v[120:121], s[10:11] op_sel_hi:[1,0]
	v_pk_mul_f32 v[130:131], v[130:131], s[10:11] op_sel_hi:[1,0]
	v_pk_mul_f32 v[122:123], v[122:123], s[10:11] op_sel_hi:[1,0]
	v_pk_mul_f32 v[128:129], v[128:129], s[10:11] op_sel_hi:[1,0]
	v_pk_fma_f32 v[118:119], v[118:119], v[132:133], v[120:121] op_sel_hi:[1,0,1]
	v_pk_fma_f32 v[120:121], v[114:115], v[132:133], v[122:123] op_sel_hi:[1,0,1]
	v_pk_fma_f32 v[114:115], v[112:113], v[132:133], v[130:131] op_sel_hi:[1,0,1]
	v_pk_fma_f32 v[116:117], v[116:117], v[132:133], v[128:129] op_sel_hi:[1,0,1]
	s_nop 0
	v_cvt_pk_bf16_f32 v112, v116, v117
	v_cvt_pk_bf16_f32 v113, v118, v119
	v_cvt_pk_bf16_f32 v114, v114, v115
	v_cvt_pk_bf16_f32 v115, v120, v121
	global_store_dwordx4 v[152:153], v[112:115], off offset:256 sc1
	v_lshl_add_u64 v[116:117], s[64:65], 0, v[124:125]
	s_waitcnt vmcnt(15)
	v_lshlrev_b32_e32 v118, 16, v168
	v_and_b32_e32 v119, 0xffff0000, v168
	v_lshlrev_b32_e32 v112, 16, v169
	v_and_b32_e32 v113, 0xffff0000, v169
	v_lshlrev_b32_e32 v120, 16, v170
	v_and_b32_e32 v121, 0xffff0000, v170
	v_lshlrev_b32_e32 v114, 16, v171
	v_and_b32_e32 v115, 0xffff0000, v171
	v_pk_mul_f32 v[112:113], v[112:113], s[10:11] op_sel_hi:[1,0]
	v_pk_mul_f32 v[120:121], v[120:121], s[10:11] op_sel_hi:[1,0]
	v_pk_mul_f32 v[114:115], v[114:115], s[10:11] op_sel_hi:[1,0]
	v_pk_mul_f32 v[118:119], v[118:119], s[10:11] op_sel_hi:[1,0]
	v_pk_fma_f32 v[110:111], v[110:111], v[132:133], v[112:113] op_sel_hi:[1,0,1]
	v_pk_fma_f32 v[112:113], v[106:107], v[132:133], v[114:115] op_sel_hi:[1,0,1]
	v_pk_fma_f32 v[106:107], v[104:105], v[132:133], v[120:121] op_sel_hi:[1,0,1]
	v_pk_fma_f32 v[108:109], v[108:109], v[132:133], v[118:119] op_sel_hi:[1,0,1]
	s_nop 0
	v_cvt_pk_bf16_f32 v104, v108, v109
	v_cvt_pk_bf16_f32 v105, v110, v111
	v_cvt_pk_bf16_f32 v106, v106, v107
	v_cvt_pk_bf16_f32 v107, v112, v113
	global_store_dwordx4 v[116:117], v[104:107], off sc1
	v_or_b32_e32 v108, 32, v138
	v_ashrrev_i32_e32 v109, 31, v108
	v_lshlrev_b64 v[108:109], 11, v[108:109]
	v_lshl_add_u64 v[108:109], v[108:109], 0, v[136:137]
	v_lshlrev_b64 v[108:109], 1, v[108:109]
	s_waitcnt vmcnt(15)
	v_lshlrev_b32_e32 v112, 16, v172
	v_and_b32_e32 v113, 0xffff0000, v172
	v_lshlrev_b32_e32 v104, 16, v173
	v_and_b32_e32 v105, 0xffff0000, v173
	v_lshlrev_b32_e32 v114, 16, v174
	v_and_b32_e32 v115, 0xffff0000, v174
	v_lshlrev_b32_e32 v106, 16, v175
	v_and_b32_e32 v107, 0xffff0000, v175
	v_pk_mul_f32 v[104:105], v[104:105], s[10:11] op_sel_hi:[1,0]
	v_pk_mul_f32 v[114:115], v[114:115], s[10:11] op_sel_hi:[1,0]
	v_pk_mul_f32 v[106:107], v[106:107], s[10:11] op_sel_hi:[1,0]
	v_pk_mul_f32 v[112:113], v[112:113], s[10:11] op_sel_hi:[1,0]
	v_pk_fma_f32 v[102:103], v[102:103], v[132:133], v[104:105] op_sel_hi:[1,0,1]
	v_pk_fma_f32 v[104:105], v[98:99], v[132:133], v[106:107] op_sel_hi:[1,0,1]
	v_pk_fma_f32 v[98:99], v[96:97], v[132:133], v[114:115] op_sel_hi:[1,0,1]
	v_pk_fma_f32 v[100:101], v[100:101], v[132:133], v[112:113] op_sel_hi:[1,0,1]
	s_nop 0
	v_cvt_pk_bf16_f32 v96, v100, v101
	v_cvt_pk_bf16_f32 v97, v102, v103
	v_cvt_pk_bf16_f32 v98, v98, v99
	v_cvt_pk_bf16_f32 v99, v104, v105
	global_store_dwordx4 v[116:117], v[96:99], off offset:256 sc1
	v_lshl_add_u64 v[100:101], s[64:65], 0, v[108:109]
	s_waitcnt vmcnt(15)
	v_lshlrev_b32_e32 v102, 16, v176
	v_and_b32_e32 v103, 0xffff0000, v176
	v_lshlrev_b32_e32 v96, 16, v177
	v_and_b32_e32 v97, 0xffff0000, v177
	v_lshlrev_b32_e32 v104, 16, v178
	v_and_b32_e32 v105, 0xffff0000, v178
	v_lshlrev_b32_e32 v98, 16, v179
	v_and_b32_e32 v99, 0xffff0000, v179
	v_pk_mul_f32 v[96:97], v[96:97], s[10:11] op_sel_hi:[1,0]
	v_pk_mul_f32 v[104:105], v[104:105], s[10:11] op_sel_hi:[1,0]
	v_pk_mul_f32 v[98:99], v[98:99], s[10:11] op_sel_hi:[1,0]
	v_pk_mul_f32 v[102:103], v[102:103], s[10:11] op_sel_hi:[1,0]
	v_pk_fma_f32 v[94:95], v[94:95], v[132:133], v[96:97] op_sel_hi:[1,0,1]
	v_pk_fma_f32 v[96:97], v[90:91], v[132:133], v[98:99] op_sel_hi:[1,0,1]
	v_pk_fma_f32 v[90:91], v[88:89], v[132:133], v[104:105] op_sel_hi:[1,0,1]
	v_pk_fma_f32 v[92:93], v[92:93], v[132:133], v[102:103] op_sel_hi:[1,0,1]
	s_nop 0
	v_cvt_pk_bf16_f32 v88, v92, v93
	v_cvt_pk_bf16_f32 v89, v94, v95
	v_cvt_pk_bf16_f32 v90, v90, v91
	v_cvt_pk_bf16_f32 v91, v96, v97
	global_store_dwordx4 v[100:101], v[88:91], off sc1
	v_or_b32_e32 v92, 48, v138
	v_ashrrev_i32_e32 v93, 31, v92
	v_lshlrev_b64 v[92:93], 11, v[92:93]
	v_lshl_add_u64 v[92:93], v[92:93], 0, v[136:137]
	v_lshlrev_b64 v[92:93], 1, v[92:93]
	s_waitcnt vmcnt(15)
	v_lshlrev_b32_e32 v96, 16, v180
	v_and_b32_e32 v97, 0xffff0000, v180
	v_lshlrev_b32_e32 v88, 16, v181
	v_and_b32_e32 v89, 0xffff0000, v181
	v_lshlrev_b32_e32 v98, 16, v182
	v_and_b32_e32 v99, 0xffff0000, v182
	v_lshlrev_b32_e32 v90, 16, v183
	v_and_b32_e32 v91, 0xffff0000, v183
	v_pk_mul_f32 v[88:89], v[88:89], s[10:11] op_sel_hi:[1,0]
	v_pk_mul_f32 v[98:99], v[98:99], s[10:11] op_sel_hi:[1,0]
	v_pk_mul_f32 v[90:91], v[90:91], s[10:11] op_sel_hi:[1,0]
	v_pk_mul_f32 v[96:97], v[96:97], s[10:11] op_sel_hi:[1,0]
	v_pk_fma_f32 v[86:87], v[86:87], v[132:133], v[88:89] op_sel_hi:[1,0,1]
	v_pk_fma_f32 v[88:89], v[82:83], v[132:133], v[90:91] op_sel_hi:[1,0,1]
	v_pk_fma_f32 v[82:83], v[80:81], v[132:133], v[98:99] op_sel_hi:[1,0,1]
	v_pk_fma_f32 v[84:85], v[84:85], v[132:133], v[96:97] op_sel_hi:[1,0,1]
	s_nop 0
	v_cvt_pk_bf16_f32 v80, v84, v85
	v_cvt_pk_bf16_f32 v81, v86, v87
	v_cvt_pk_bf16_f32 v82, v82, v83
	v_cvt_pk_bf16_f32 v83, v88, v89
	global_store_dwordx4 v[100:101], v[80:83], off offset:256 sc1
	v_lshl_add_u64 v[84:85], s[64:65], 0, v[92:93]
	s_waitcnt vmcnt(15)
	v_lshlrev_b32_e32 v86, 16, v184
	v_and_b32_e32 v87, 0xffff0000, v184
	v_lshlrev_b32_e32 v80, 16, v185
	v_and_b32_e32 v81, 0xffff0000, v185
	v_lshlrev_b32_e32 v88, 16, v186
	v_and_b32_e32 v89, 0xffff0000, v186
	v_lshlrev_b32_e32 v82, 16, v187
	v_and_b32_e32 v83, 0xffff0000, v187
	v_pk_mul_f32 v[80:81], v[80:81], s[10:11] op_sel_hi:[1,0]
	v_pk_mul_f32 v[88:89], v[88:89], s[10:11] op_sel_hi:[1,0]
	v_pk_mul_f32 v[82:83], v[82:83], s[10:11] op_sel_hi:[1,0]
	v_pk_mul_f32 v[86:87], v[86:87], s[10:11] op_sel_hi:[1,0]
	v_pk_fma_f32 v[78:79], v[78:79], v[132:133], v[80:81] op_sel_hi:[1,0,1]
	v_pk_fma_f32 v[80:81], v[74:75], v[132:133], v[82:83] op_sel_hi:[1,0,1]
	v_pk_fma_f32 v[74:75], v[72:73], v[132:133], v[88:89] op_sel_hi:[1,0,1]
	v_pk_fma_f32 v[76:77], v[76:77], v[132:133], v[86:87] op_sel_hi:[1,0,1]
	s_nop 0
	v_cvt_pk_bf16_f32 v72, v76, v77
	v_cvt_pk_bf16_f32 v73, v78, v79
	v_cvt_pk_bf16_f32 v74, v74, v75
	v_cvt_pk_bf16_f32 v75, v80, v81
	global_store_dwordx4 v[84:85], v[72:75], off sc1
	v_lshl_add_u64 v[76:77], v[134:135], 0, s[12:13]
	s_waitcnt vmcnt(15)
	v_lshlrev_b32_e32 v80, 16, v188
	v_and_b32_e32 v81, 0xffff0000, v188
	v_lshlrev_b32_e32 v72, 16, v189
	v_and_b32_e32 v73, 0xffff0000, v189
	v_lshlrev_b32_e32 v82, 16, v190
	v_and_b32_e32 v83, 0xffff0000, v190
	v_lshlrev_b32_e32 v74, 16, v191
	v_and_b32_e32 v75, 0xffff0000, v191
	v_pk_mul_f32 v[72:73], v[72:73], s[10:11] op_sel_hi:[1,0]
	v_pk_mul_f32 v[82:83], v[82:83], s[10:11] op_sel_hi:[1,0]
	v_pk_mul_f32 v[74:75], v[74:75], s[10:11] op_sel_hi:[1,0]
	v_pk_mul_f32 v[80:81], v[80:81], s[10:11] op_sel_hi:[1,0]
	v_pk_fma_f32 v[70:71], v[70:71], v[132:133], v[72:73] op_sel_hi:[1,0,1]
	v_pk_fma_f32 v[72:73], v[66:67], v[132:133], v[74:75] op_sel_hi:[1,0,1]
	v_pk_fma_f32 v[66:67], v[64:65], v[132:133], v[82:83] op_sel_hi:[1,0,1]
	v_pk_fma_f32 v[68:69], v[68:69], v[132:133], v[80:81] op_sel_hi:[1,0,1]
	s_nop 0
	v_cvt_pk_bf16_f32 v64, v68, v69
	v_cvt_pk_bf16_f32 v65, v70, v71
	v_cvt_pk_bf16_f32 v66, v66, v67
	v_cvt_pk_bf16_f32 v67, v72, v73
	global_store_dwordx4 v[84:85], v[64:67], off offset:256 sc1
	v_lshl_add_u64 v[68:69], s[64:65], 0, v[76:77]
	s_waitcnt vmcnt(15)
	v_lshlrev_b32_e32 v70, 16, v192
	v_and_b32_e32 v71, 0xffff0000, v192
	v_lshlrev_b32_e32 v64, 16, v193
	v_and_b32_e32 v65, 0xffff0000, v193
	v_lshlrev_b32_e32 v72, 16, v194
	v_and_b32_e32 v73, 0xffff0000, v194
	v_lshlrev_b32_e32 v66, 16, v195
	v_and_b32_e32 v67, 0xffff0000, v195
	v_pk_mul_f32 v[64:65], v[64:65], s[10:11] op_sel_hi:[1,0]
	v_pk_mul_f32 v[72:73], v[72:73], s[10:11] op_sel_hi:[1,0]
	v_pk_mul_f32 v[66:67], v[66:67], s[10:11] op_sel_hi:[1,0]
	v_pk_mul_f32 v[70:71], v[70:71], s[10:11] op_sel_hi:[1,0]
	v_pk_fma_f32 v[62:63], v[62:63], v[132:133], v[64:65] op_sel_hi:[1,0,1]
	v_pk_fma_f32 v[64:65], v[58:59], v[132:133], v[66:67] op_sel_hi:[1,0,1]
	v_pk_fma_f32 v[58:59], v[56:57], v[132:133], v[72:73] op_sel_hi:[1,0,1]
	v_pk_fma_f32 v[60:61], v[60:61], v[132:133], v[70:71] op_sel_hi:[1,0,1]
	s_nop 0
	v_cvt_pk_bf16_f32 v56, v60, v61
	v_cvt_pk_bf16_f32 v57, v62, v63
	v_cvt_pk_bf16_f32 v58, v58, v59
	v_cvt_pk_bf16_f32 v59, v64, v65
	global_store_dwordx4 v[68:69], v[56:59], off sc1
	v_lshl_add_u64 v[60:61], v[134:135], 0, s[14:15]
	s_waitcnt vmcnt(15)
	v_lshlrev_b32_e32 v64, 16, v196
	v_and_b32_e32 v65, 0xffff0000, v196
	v_lshlrev_b32_e32 v56, 16, v197
	v_and_b32_e32 v57, 0xffff0000, v197
	v_lshlrev_b32_e32 v66, 16, v198
	v_and_b32_e32 v67, 0xffff0000, v198
	v_lshlrev_b32_e32 v58, 16, v199
	v_and_b32_e32 v59, 0xffff0000, v199
	v_pk_mul_f32 v[56:57], v[56:57], s[10:11] op_sel_hi:[1,0]
	v_pk_mul_f32 v[66:67], v[66:67], s[10:11] op_sel_hi:[1,0]
	v_pk_mul_f32 v[58:59], v[58:59], s[10:11] op_sel_hi:[1,0]
	v_pk_mul_f32 v[64:65], v[64:65], s[10:11] op_sel_hi:[1,0]
	v_pk_fma_f32 v[54:55], v[54:55], v[132:133], v[56:57] op_sel_hi:[1,0,1]
	v_pk_fma_f32 v[56:57], v[50:51], v[132:133], v[58:59] op_sel_hi:[1,0,1]
	v_pk_fma_f32 v[50:51], v[48:49], v[132:133], v[66:67] op_sel_hi:[1,0,1]
	v_pk_fma_f32 v[52:53], v[52:53], v[132:133], v[64:65] op_sel_hi:[1,0,1]
	s_nop 0
	v_cvt_pk_bf16_f32 v48, v52, v53
	v_cvt_pk_bf16_f32 v49, v54, v55
	v_cvt_pk_bf16_f32 v50, v50, v51
	v_cvt_pk_bf16_f32 v51, v56, v57
	global_store_dwordx4 v[68:69], v[48:51], off offset:256 sc1
	v_lshl_add_u64 v[52:53], s[64:65], 0, v[60:61]
	s_waitcnt vmcnt(15)
	v_lshlrev_b32_e32 v54, 16, v200
	v_and_b32_e32 v55, 0xffff0000, v200
	v_lshlrev_b32_e32 v48, 16, v201
	v_and_b32_e32 v49, 0xffff0000, v201
	v_lshlrev_b32_e32 v56, 16, v202
	v_and_b32_e32 v57, 0xffff0000, v202
	v_lshlrev_b32_e32 v50, 16, v203
	v_and_b32_e32 v51, 0xffff0000, v203
	v_pk_mul_f32 v[48:49], v[48:49], s[10:11] op_sel_hi:[1,0]
	v_pk_mul_f32 v[56:57], v[56:57], s[10:11] op_sel_hi:[1,0]
	v_pk_mul_f32 v[50:51], v[50:51], s[10:11] op_sel_hi:[1,0]
	v_pk_mul_f32 v[54:55], v[54:55], s[10:11] op_sel_hi:[1,0]
	v_pk_fma_f32 v[46:47], v[46:47], v[132:133], v[48:49] op_sel_hi:[1,0,1]
	v_pk_fma_f32 v[48:49], v[42:43], v[132:133], v[50:51] op_sel_hi:[1,0,1]
	v_pk_fma_f32 v[42:43], v[40:41], v[132:133], v[56:57] op_sel_hi:[1,0,1]
	v_pk_fma_f32 v[44:45], v[44:45], v[132:133], v[54:55] op_sel_hi:[1,0,1]
	s_nop 0
	v_cvt_pk_bf16_f32 v40, v44, v45
	v_cvt_pk_bf16_f32 v41, v46, v47
	v_cvt_pk_bf16_f32 v42, v42, v43
	v_cvt_pk_bf16_f32 v43, v48, v49
	global_store_dwordx4 v[52:53], v[40:43], off sc1
	v_lshl_add_u64 v[44:45], v[134:135], 0, s[16:17]
	s_waitcnt vmcnt(15)
	v_lshlrev_b32_e32 v48, 16, v204
	v_and_b32_e32 v49, 0xffff0000, v204
	v_lshlrev_b32_e32 v40, 16, v205
	v_and_b32_e32 v41, 0xffff0000, v205
	v_lshlrev_b32_e32 v50, 16, v206
	v_and_b32_e32 v51, 0xffff0000, v206
	v_lshlrev_b32_e32 v42, 16, v207
	v_and_b32_e32 v43, 0xffff0000, v207
	v_pk_mul_f32 v[40:41], v[40:41], s[10:11] op_sel_hi:[1,0]
	v_pk_mul_f32 v[50:51], v[50:51], s[10:11] op_sel_hi:[1,0]
	v_pk_mul_f32 v[42:43], v[42:43], s[10:11] op_sel_hi:[1,0]
	v_pk_mul_f32 v[48:49], v[48:49], s[10:11] op_sel_hi:[1,0]
	v_pk_fma_f32 v[38:39], v[38:39], v[132:133], v[40:41] op_sel_hi:[1,0,1]
	v_pk_fma_f32 v[40:41], v[34:35], v[132:133], v[42:43] op_sel_hi:[1,0,1]
	v_pk_fma_f32 v[34:35], v[32:33], v[132:133], v[50:51] op_sel_hi:[1,0,1]
	v_pk_fma_f32 v[36:37], v[36:37], v[132:133], v[48:49] op_sel_hi:[1,0,1]
	s_nop 0
	v_cvt_pk_bf16_f32 v32, v36, v37
	v_cvt_pk_bf16_f32 v33, v38, v39
	v_cvt_pk_bf16_f32 v34, v34, v35
	v_cvt_pk_bf16_f32 v35, v40, v41
	global_store_dwordx4 v[52:53], v[32:35], off offset:256 sc1
	v_lshl_add_u64 v[36:37], s[64:65], 0, v[44:45]
	s_waitcnt vmcnt(15)
	v_lshlrev_b32_e32 v38, 16, v208
	v_and_b32_e32 v39, 0xffff0000, v208
	v_lshlrev_b32_e32 v32, 16, v209
	v_and_b32_e32 v33, 0xffff0000, v209
	v_lshlrev_b32_e32 v40, 16, v210
	v_and_b32_e32 v41, 0xffff0000, v210
	v_lshlrev_b32_e32 v34, 16, v211
	v_and_b32_e32 v35, 0xffff0000, v211
	v_pk_mul_f32 v[32:33], v[32:33], s[10:11] op_sel_hi:[1,0]
	v_pk_mul_f32 v[40:41], v[40:41], s[10:11] op_sel_hi:[1,0]
	v_pk_mul_f32 v[34:35], v[34:35], s[10:11] op_sel_hi:[1,0]
	v_pk_mul_f32 v[38:39], v[38:39], s[10:11] op_sel_hi:[1,0]
	v_pk_fma_f32 v[30:31], v[30:31], v[132:133], v[32:33] op_sel_hi:[1,0,1]
	v_pk_fma_f32 v[32:33], v[26:27], v[132:133], v[34:35] op_sel_hi:[1,0,1]
	v_pk_fma_f32 v[26:27], v[24:25], v[132:133], v[40:41] op_sel_hi:[1,0,1]
	v_pk_fma_f32 v[28:29], v[28:29], v[132:133], v[38:39] op_sel_hi:[1,0,1]
	s_nop 0
	v_cvt_pk_bf16_f32 v24, v28, v29
	v_cvt_pk_bf16_f32 v25, v30, v31
	v_cvt_pk_bf16_f32 v26, v26, v27
	v_cvt_pk_bf16_f32 v27, v32, v33
	global_store_dwordx4 v[36:37], v[24:27], off sc1
	v_lshl_add_u64 v[28:29], v[134:135], 0, s[18:19]
	s_waitcnt vmcnt(15)
	v_lshlrev_b32_e32 v32, 16, v212
	v_and_b32_e32 v33, 0xffff0000, v212
	v_lshlrev_b32_e32 v24, 16, v213
	v_and_b32_e32 v25, 0xffff0000, v213
	v_lshlrev_b32_e32 v34, 16, v214
	v_and_b32_e32 v35, 0xffff0000, v214
	v_lshlrev_b32_e32 v26, 16, v215
	v_and_b32_e32 v27, 0xffff0000, v215
	v_pk_mul_f32 v[24:25], v[24:25], s[10:11] op_sel_hi:[1,0]
	v_pk_mul_f32 v[34:35], v[34:35], s[10:11] op_sel_hi:[1,0]
	v_pk_mul_f32 v[26:27], v[26:27], s[10:11] op_sel_hi:[1,0]
	v_pk_mul_f32 v[32:33], v[32:33], s[10:11] op_sel_hi:[1,0]
	v_pk_fma_f32 v[22:23], v[22:23], v[132:133], v[24:25] op_sel_hi:[1,0,1]
	v_pk_fma_f32 v[24:25], v[18:19], v[132:133], v[26:27] op_sel_hi:[1,0,1]
	v_pk_fma_f32 v[18:19], v[16:17], v[132:133], v[34:35] op_sel_hi:[1,0,1]
	v_pk_fma_f32 v[20:21], v[20:21], v[132:133], v[32:33] op_sel_hi:[1,0,1]
	s_nop 0
	v_cvt_pk_bf16_f32 v16, v20, v21
	v_cvt_pk_bf16_f32 v17, v22, v23
	v_cvt_pk_bf16_f32 v18, v18, v19
	v_cvt_pk_bf16_f32 v19, v24, v25
	global_store_dwordx4 v[36:37], v[16:19], off offset:256 sc1
	v_lshl_add_u64 v[20:21], s[64:65], 0, v[28:29]
	s_waitcnt vmcnt(15)
	v_lshlrev_b32_e32 v22, 16, v216
	v_and_b32_e32 v23, 0xffff0000, v216
	v_lshlrev_b32_e32 v16, 16, v217
	v_and_b32_e32 v17, 0xffff0000, v217
	v_lshlrev_b32_e32 v24, 16, v218
	v_and_b32_e32 v25, 0xffff0000, v218
	v_lshlrev_b32_e32 v18, 16, v219
	v_and_b32_e32 v19, 0xffff0000, v219
	v_pk_mul_f32 v[16:17], v[16:17], s[10:11] op_sel_hi:[1,0]
	v_pk_mul_f32 v[24:25], v[24:25], s[10:11] op_sel_hi:[1,0]
	v_pk_mul_f32 v[18:19], v[18:19], s[10:11] op_sel_hi:[1,0]
	v_pk_mul_f32 v[22:23], v[22:23], s[10:11] op_sel_hi:[1,0]
	v_pk_fma_f32 v[14:15], v[14:15], v[132:133], v[16:17] op_sel_hi:[1,0,1]
	v_pk_fma_f32 v[16:17], v[10:11], v[132:133], v[18:19] op_sel_hi:[1,0,1]
	v_pk_fma_f32 v[10:11], v[8:9], v[132:133], v[24:25] op_sel_hi:[1,0,1]
	v_pk_fma_f32 v[12:13], v[12:13], v[132:133], v[22:23] op_sel_hi:[1,0,1]
	s_nop 0
	v_cvt_pk_bf16_f32 v8, v12, v13
	v_cvt_pk_bf16_f32 v9, v14, v15
	v_cvt_pk_bf16_f32 v10, v10, v11
	v_cvt_pk_bf16_f32 v11, v16, v17
	global_store_dwordx4 v[20:21], v[8:11], off sc1
	s_waitcnt vmcnt(15)
	v_lshlrev_b32_e32 v12, 16, v220
	v_and_b32_e32 v13, 0xffff0000, v220
	v_lshlrev_b32_e32 v8, 16, v221
	v_and_b32_e32 v9, 0xffff0000, v221
	v_lshlrev_b32_e32 v14, 16, v222
	v_and_b32_e32 v15, 0xffff0000, v222
	v_lshlrev_b32_e32 v10, 16, v223
	v_and_b32_e32 v11, 0xffff0000, v223
	v_pk_mul_f32 v[8:9], v[8:9], s[10:11] op_sel_hi:[1,0]
	v_pk_mul_f32 v[14:15], v[14:15], s[10:11] op_sel_hi:[1,0]
	v_pk_mul_f32 v[10:11], v[10:11], s[10:11] op_sel_hi:[1,0]
	v_pk_mul_f32 v[12:13], v[12:13], s[10:11] op_sel_hi:[1,0]
	v_pk_fma_f32 v[6:7], v[6:7], v[132:133], v[8:9] op_sel_hi:[1,0,1]
	v_pk_fma_f32 v[8:9], v[2:3], v[132:133], v[10:11] op_sel_hi:[1,0,1]
	v_pk_fma_f32 v[2:3], v[0:1], v[132:133], v[14:15] op_sel_hi:[1,0,1]
	v_pk_fma_f32 v[4:5], v[4:5], v[132:133], v[12:13] op_sel_hi:[1,0,1]
	s_nop 0
	v_cvt_pk_bf16_f32 v0, v4, v5
	v_cvt_pk_bf16_f32 v1, v6, v7
	v_cvt_pk_bf16_f32 v2, v2, v3
	v_cvt_pk_bf16_f32 v3, v8, v9
	global_store_dwordx4 v[20:21], v[0:3], off offset:256 sc1
	s_cbranch_vccnz .LBB0_1614
	s_andn2_b64 vcc, exec, s[4:5]
	s_cbranch_vccnz .LBB0_1613
	s_barrier
	s_branch .LBB0_1613
